# attention blocks: one static priority raise for waves 4-7, reset after the attention loop
# baseline (speedup 1.0000x reference)
; #define SUB(n) if constexpr ((SUBMASK >> (n)) & 1)
; DEVI int obid() { int b = blockIdx.x; asm volatile("" : "+s"(b)); return b; }
; DEVI void phase_l4(const Params& p, int l, char* smem) {
;     ...
; #pragma nounroll
;     for (int rep = 0; rep < L4_ATT_REP; ++rep)
; #pragma nounroll
;     for (int it = 0; ; ++it) {
;         int u;
;         if (!spec) { u = obid() + it * gridDim.x; if (u >= nal + nac) break; }
;         else { if (it >= 2) break; u = (it == 0) ? obid() : (obid() < nac ? nal + obid() : (dbl ? obid() + L4NC : -1)); if (u < 0) break; }
;         if (u < nal) { SUB(4) {
;             const int bh = u >> 3, qb = u & 7, b = bh >> 3, h = bh & 7;
;             att::attn_body(Q + ((size_t)bh * KEYS + CL + qb * 256) * 192, Kb + (size_t)bh * KEYS * 192, Vb + (size_t)bh * KEYS * 128,
;                            ymix + (size_t)(b * SEQ + qb * 256) * DM + h * 128, KEYS, smem);
.LBB0_644:
	v_readfirstlane_b32 s4, v0
	s_nop 3
	s_lshr_b32 s4, s4, 8
	s_cmp_lg_u32 s4, 0
	s_cbranch_scc0 .Lattn_prio_skip
	s_setprio 1

; DEVI void phase_l4(const Params& p, int l, char* smem) {
;     ...
;     if (dbl) return;
;     if (threadIdx.x == 0) {
;         unsigned* c = (unsigned*)(p.ws + WS_BAR) + PFXCNT_WORD + 64 * l; unsigned sp = 0;
;         while (__hip_atomic_load(c, __ATOMIC_RELAXED, __HIP_MEMORY_SCOPE_AGENT) < gridDim.x) { __builtin_amdgcn_s_sleep(2); if (++sp > (1u << 22)) break; }
;         __builtin_amdgcn_fence(__ATOMIC_ACQUIRE, "agent");
;         asm volatile("s_waitcnt vmcnt(0)" ::: "memory");
;     }
;     __syncthreads();
.LBB0_679:
	s_setprio 0
	s_andn2_b64 vcc, exec, s[50:51]
	s_cbranch_vccnz .LBB0_772
	s_mov_b64 s[16:17], exec
	v_readlane_b32 s4, v253, 0
	v_readlane_b32 s5, v253, 1
	s_and_b64 s[4:5], s[16:17], s[4:5]
	s_mov_b64 exec, s[4:5]
	s_cbranch_execz .LBB0_690
	v_readlane_b32 s4, v254, 61
	v_readlane_b32 s5, v254, 62
	s_lshl_b32 s52, s4, 6
	s_lshl_b64 s[4:5], s[52:53], 2
	v_readlane_b32 s6, v254, 14
	s_add_u32 s28, s6, s4
	v_readlane_b32 s4, v254, 15
	s_addc_u32 s29, s4, s5
	s_mov_b32 s4, 0x400001
	s_branch .LBB0_683
